# FFN-up epilogue: row scales and per-channel parameter block fetched one tile ahead into otherwise unused registers, first vmcnt(0) of the epilogue removed
# speedup vs baseline: 1.0064x; 1.0009x over previous
.LBB0_1639:
	s_lshl_b32 s3, s3, 5
	s_mov_b64 s[14:15], 0x80
	s_and_b32 s56, s3, 0x60
	s_add_i32 m0, s50, 0x18000
	v_lshl_add_u64 v[8:9], v[8:9], 0, s[14:15]
	s_lshl_b32 s55, s2, 6
	s_lshl_b32 s1, s2, 13
	s_lshl_b32 s3, s56, 7
	s_waitcnt vmcnt(2)
	s_barrier
	global_load_lds_dwordx4 v[8:9], off
	v_lshl_add_u64 v[6:7], v[6:7], 0, s[14:15]
	s_add_i32 m0, s50, 0x1a000
	s_add_i32 s57, s50, 0x8000
	s_add_i32 s58, s50, 0xa000
	global_load_lds_dwordx4 v[6:7], off
	v_lshl_add_u64 v[2:3], v[2:3], 0, s[14:15]
	s_mov_b32 m0, s57
	s_add_u32 s16, s42, 0x80080
	global_load_lds_dwordx4 v[2:3], off
	v_lshl_add_u64 v[2:3], v[4:5], 0, s[14:15]
	s_mov_b32 m0, s58
	s_addc_u32 s17, s43, 0
	global_load_lds_dwordx4 v[2:3], off
	s_add_i32 m0, s50, 0x1c000
	v_lshl_add_u64 v[2:3], s[16:17], 0, v[150:151]
	global_load_lds_dwordx4 v[2:3], off
	v_lshl_add_u64 v[2:3], s[16:17], 0, v[154:155]
	s_add_i32 m0, s50, 0x1e000
	v_and_b32_e32 v1, 48, v0
	global_load_lds_dwordx4 v[2:3], off
	v_lshlrev_b32_e32 v2, 6, v0
	s_movk_i32 s16, 0x3c0
	s_cmpk_lt_u32 s18, 0x100
	v_and_or_b32 v1, v2, s16, v1
	s_cselect_b64 s[16:17], -1, 0
	s_lshl_b32 s59, s2, 1
	v_lshlrev_b32_e32 v2, 2, v0
	s_add_i32 s59, s59, 0x3ffff2
	v_and_b32_e32 v2, 32, v2
	s_cmpk_gt_u32 s18, 0xff
	v_bitop3_b32 v3, v1, s1, v2 bitop3:0xde
	v_bitop3_b32 v1, s3, v1, v2 bitop3:0xf6
	s_cselect_b64 s[18:19], -1, 0
	s_lshl_b32 s60, s2, 2
	v_lshlrev_b32_e32 v2, 9, v0
	s_add_i32 s61, s60, 8
	s_ashr_i32 s62, s91, 31
	s_ashr_i32 s63, s90, 31
	v_and_b32_e32 v2, 0x30000, v2
	v_lshlrev_b32_e32 v4, 12, v12
	s_add_u32 s20, s68, 0xc00000
	v_or3_b32 v2, v10, v2, v4
	s_addc_u32 s21, s69, 0
	v_add_u32_e32 v158, v2, v11
	v_lshlrev_b32_e32 v2, 5, v13
	s_waitcnt vmcnt(6)
	s_add_u32 s22, s68, 0xc40000
	v_and_b32_e32 v2, 0x70000, v2
	s_addc_u32 s23, s69, 0
	v_or3_b32 v2, v10, v2, v4
	s_add_i32 s64, 0, 0x10000
	s_add_i32 s65, 0, 0x14000
	s_movk_i32 s24, 0xfc00
	v_mov_b32_e32 v159, v157
	v_add_u32_e32 v160, v2, v11
	v_mov_b32_e32 v161, v157
	v_mov_b64_e32 v[162:163], 0x15d6
	v_mov_b64_e32 v[164:165], 0x15d5
	v_add_u32_e32 v167, s64, v1
	v_add_u32_e32 v228, s65, v1
	v_add_u32_e32 v229, 0, v3
	s_movk_i32 s66, 0x160
	s_movk_i32 s67, 0x7f
	s_movk_i32 s72, 0x5600
	s_mov_b32 s73, 0xac00
	s_mov_b32 s25, -1
	s_movk_i32 s74, 0x2b00
	s_add_i32 s75, 0, 0x20000
	s_add_i32 s76, 0, 0x21000
	v_mov_b32_e32 v230, 0xac00
	s_barrier
	v_lshrrev_b32_e32 v250, 5, v0
	v_and_b32_e32 v251, 31, v0
	v_lshlrev_b32_e32 v251, 4, v251
	v_add_u32_e32 v248, -4, v250
	v_lshrrev_b32_e32 v248, 1, v248
	v_mul_u32_u24_e32 v248, 0x15800, v248
	v_and_b32_e32 v249, 1, v250
	v_mul_u32_u24_e32 v249, 0xac00, v249
	v_add3_u32 v248, v248, v249, v251
	v_mul_u32_u24_e32 v249, 0xac00, v250
	v_add_u32_e32 v249, v249, v251
	v_add_u32_e32 v247, -2, v250
	v_lshl_add_u32 v247, v247, 9, v251
	v_mov_b32_e32 v231, 0x200
	v_mov_b32_e32 v252, s80
	v_mov_b32_e32 v253, s81
	v_mov_b32_e32 v246, v248
	v_cmp_gt_u32_e32 vcc, 4, v250
	v_mov_b32_e32 v244, s22
	v_mov_b32_e32 v245, s23
	v_mov_b32_e32 v243, 0x400
	v_cndmask_b32_e32 v252, v252, v244, vcc
	v_cndmask_b32_e32 v253, v253, v245, vcc
	v_cndmask_b32_e32 v246, v246, v247, vcc
	v_cndmask_b32_e32 v231, v231, v243, vcc
	v_cmp_gt_u32_e32 vcc, 2, v250
	v_mov_b32_e32 v244, s82
	v_mov_b32_e32 v245, s83
	v_mov_b32_e32 v243, 0x200
	v_cndmask_b32_e32 v252, v252, v244, vcc
	v_cndmask_b32_e32 v253, v253, v245, vcc
	v_cndmask_b32_e32 v246, v246, v249, vcc
	v_cndmask_b32_e32 v231, v231, v243, vcc
	v_cmp_lt_u32_e32 vcc, 10, v250
	s_nop 1
	v_cndmask_b32_e32 v252, v252, v244, vcc
	v_cndmask_b32_e32 v253, v253, v245, vcc
	v_cndmask_b32_e32 v246, v246, v251, vcc
	v_cndmask_b32_e32 v231, v231, v243, vcc
	v_mov_b32_e32 v247, 0
	v_lshl_add_u64 v[252:253], v[246:247], 0, v[252:253]
	v_mov_b32_e32 v250, s0
	v_min_u32_e32 v250, 0x55, v250
	v_mul_u32_u24_e32 v250, v250, v231
	v_mov_b32_e32 v251, 0
	v_lshl_add_u64 v[248:249], v[250:251], 0, v[252:253]
	global_load_dwordx4 v[248:251], v[248:249], off
	v_mov_b32_e32 v246, s40
	v_min_u32_e32 v246, 64, v246
	v_lshl_add_u32 v246, v246, 8, s55
	v_and_or_b32 v246, v166, 15, v246
	v_lshlrev_b32_e32 v246, 2, v246
	global_load_dword v240, v246, s[20:21]
	global_load_dword v241, v246, s[20:21] offset:64
	global_load_dword v242, v246, s[20:21] offset:128
	global_load_dword v243, v246, s[20:21] offset:192
	global_load_dword v244, v246, s[20:21] offset:512
	global_load_dword v245, v246, s[20:21] offset:576
	global_load_dword v247, v246, s[20:21] offset:704
	global_load_dword v246, v246, s[20:21] offset:640
	s_branch .LBB0_1642

.LBB0_1652:
	v_mov_b32_e32 v130, v166
	s_lshl_b32 s1, s40, 8
	v_and_b32_e32 v193, 15, v130
	v_lshrrev_b32_e32 v130, 1, v130
	v_and_b32_e32 v130, 0x7ffffff8, v130
	v_add_u32_e32 v144, s56, v130
	s_lshl_b32 s34, s0, 7
	s_add_i32 s1, s1, s55
	v_add_u32_e32 v130, s34, v144
	v_or_b32_e32 v169, s1, v193
	v_mov_b32_e32 v156, v130
	v_add_u32_e32 v192, s34, v130
	v_mov_b32_e32 v130, v169
	v_mov_b32_e32 v131, v157
	v_lshl_add_u64 v[132:133], v[130:131], 2, s[20:21]
	v_add_u32_e32 v134, 16, v130
	v_mov_b32_e32 v135, v157
	v_add_u32_e32 v136, 32, v130
	v_mov_b32_e32 v137, v157
	v_add_u32_e32 v138, 48, v130
	v_mov_b32_e32 v139, v157
	v_add_u32_e32 v140, 0x80, v130
	v_mov_b32_e32 v141, v157
	v_add_u32_e32 v142, 0x90, v130
	v_mov_b32_e32 v143, v157
	v_add_u32_e32 v146, 0xa0, v130
	v_mov_b32_e32 v147, v157
	v_add_u32_e32 v130, 0xb0, v130
	v_lshl_add_u64 v[134:135], v[134:135], 2, s[20:21]
	v_lshl_add_u64 v[136:137], v[136:137], 2, s[20:21]
	v_lshl_add_u64 v[138:139], v[138:139], 2, s[20:21]
	v_lshl_add_u64 v[140:141], v[140:141], 2, s[20:21]
	v_lshl_add_u64 v[142:143], v[142:143], 2, s[20:21]
	v_lshl_add_u64 v[146:147], v[146:147], 2, s[20:21]
	v_lshl_add_u64 v[130:131], v[130:131], 2, s[20:21]
	v_mov_b32_e32 v172, v240
	v_mov_b32_e32 v170, v241
	v_mov_b32_e32 v168, v242
	v_mov_b32_e32 v174, v243
	v_mov_b32_e32 v208, v244
	v_mov_b32_e32 v206, v245
	v_mov_b32_e32 v198, v246
	v_mov_b32_e32 v194, v247
	v_mov_b32_e32 v132, v0
	s_nop 0
	v_cmp_gt_u32_e32 vcc, s66, v132
	s_and_saveexec_b64 s[42:43], vcc
	s_cbranch_execz .LBB0_1662
	v_lshrrev_b32_e32 v133, 5, v132
	v_cmp_lt_u32_e32 vcc, 63, v132
	s_and_saveexec_b64 s[38:39], vcc
	s_xor_b64 s[44:45], exec, s[38:39]
	s_cbranch_execz .LBB0_1659
	v_cmp_lt_u32_e32 vcc, s67, v132
	s_and_saveexec_b64 s[38:39], vcc
	s_xor_b64 s[46:47], exec, s[38:39]
	s_cbranch_execz .LBB0_1656
	v_add_u32_e32 v130, -4, v133
	v_lshrrev_b32_e32 v130, 1, v130
	v_and_b32_e32 v133, 32, v132
	v_mul_lo_u32 v130, v130, s72
	v_mov_b32_e32 v131, v157
	v_cmp_ne_u32_e32 vcc, 0, v133
	v_lshl_add_u64 v[130:131], v[130:131], 2, s[80:81]
	v_mov_b32_e32 v135, v157
	v_cndmask_b32_e32 v134, 0, v230, vcc
	v_lshl_add_u64 v[130:131], v[130:131], 0, v[134:135]
	s_ashr_i32 s35, s34, 31
	v_lshl_add_u64 v[130:131], s[34:35], 2, v[130:131]

.LBB0_1659:
	s_andn2_saveexec_b64 s[0:1], s[44:45]
	v_mul_lo_u32 v130, v133, s74
	v_mov_b32_e32 v131, v157
	v_lshl_add_u64 v[130:131], v[130:131], 2, s[82:83]
	s_ashr_i32 s35, s34, 31
	v_lshl_add_u64 v[130:131], s[34:35], 2, v[130:131]
	s_or_b64 exec, exec, s[0:1]
	v_lshlrev_b32_e32 v134, 4, v132
	v_and_b32_e32 v132, 0x1f0, v134
	v_mov_b32_e32 v133, v157
	v_lshl_add_u64 v[130:131], v[130:131], 0, v[132:133]
	s_nop 0
	v_add_u32_e32 v134, 0, v134
	v_add_u32_e32 v134, 0x22000, v134
	ds_write_b128 v134, v[248:251]

.LBB0_1669:
	s_or_b64 exec, exec, s[34:35]
	v_or_b32_e32 v103, 0xffffffe0, v102
	v_add_u32_e32 v102, s60, v103
	v_lshl_add_u32 v195, v144, 2, s75
	s_and_b64 s[40:41], s[18:19], vcc
	v_mov_b32_e32 v108, 0
	v_lshl_add_u32 v171, v102, 9, v195
	v_mov_b32_e32 v144, 0
	v_mov_b32_e32 v145, 0
	v_mov_b32_e32 v146, 0
	v_mov_b32_e32 v147, 0
	s_and_saveexec_b64 s[34:35], s[40:41]
	ds_read_b128 v[144:147], v171
	s_or_b64 exec, exec, s[34:35]
	v_mov_b32_e32 v109, 0
	v_mov_b32_e32 v110, 0
	v_mov_b32_e32 v111, 0
	s_and_saveexec_b64 s[34:35], s[40:41]
	ds_read_b128 v[108:111], v171 offset:512
	s_or_b64 exec, exec, s[34:35]
	s_waitcnt lgkmcnt(0)
	v_pk_mul_f32 v[222:223], v[128:129], v[140:141]
	v_pk_mul_f32 v[224:225], v[128:129], v[136:137]
	v_pk_mul_f32 v[226:227], v[128:129], v[132:133]
	v_pk_mul_f32 v[124:125], v[112:113], v[124:125]
	v_pk_mul_f32 v[128:129], v[114:115], v[122:123]
	v_pk_mul_f32 v[120:121], v[112:113], v[120:121]
	v_pk_mul_f32 v[122:123], v[112:113], v[116:117]
	v_cvt_f32_i32_e32 v113, v22
	v_cvt_f32_i32_e32 v112, v46
	s_nop 0
	s_nop 0
	v_pk_mul_f32 v[142:143], v[130:131], v[142:143]
	v_pk_mul_f32 v[220:221], v[130:131], v[138:139]
	v_pk_mul_f32 v[140:141], v[130:131], v[134:135]
	v_pk_mul_f32 v[130:131], v[114:115], v[118:119]
	s_nop 0
	v_mov_b32_dpp v116, v144 row_ror:2 row_mask:0xf bank_mask:0xf
	s_nop 0
	v_mov_b32_dpp v117, v108 row_ror:2 row_mask:0xf bank_mask:0xf
	s_waitcnt vmcnt(0)
	v_mov_b32_e32 v250, s26
	v_min_u32_e32 v250, 0x55, v250
	v_mul_u32_u24_e32 v250, v250, v231
	v_mov_b32_e32 v251, 0
	v_lshl_add_u64 v[248:249], v[250:251], 0, v[252:253]
	global_load_dwordx4 v[248:251], v[248:249], off
	v_mov_b32_e32 v246, s28
	v_min_u32_e32 v246, 64, v246
	v_lshl_add_u32 v246, v246, 8, s55
	v_and_or_b32 v246, v166, 15, v246
	v_lshlrev_b32_e32 v246, 2, v246
	global_load_dword v240, v246, s[20:21]
	global_load_dword v241, v246, s[20:21] offset:64
	global_load_dword v242, v246, s[20:21] offset:128
	global_load_dword v243, v246, s[20:21] offset:192
	global_load_dword v244, v246, s[20:21] offset:512
	global_load_dword v245, v246, s[20:21] offset:576
	global_load_dword v247, v246, s[20:21] offset:704
	global_load_dword v246, v246, s[20:21] offset:640
	v_pk_mul_f32 v[236:237], v[172:173], v[112:113] op_sel_hi:[0,1]
	v_pk_mul_f32 v[126:127], v[114:115], v[126:127]
	v_mov_b32_dpp v118, v144 row_ror:1 row_mask:0xf bank_mask:0xf
	s_nop 0
	s_nop 0
	s_nop 0
	s_nop 0
	v_mov_b32_dpp v119, v108 row_ror:1 row_mask:0xf bank_mask:0xf
	v_mov_b32_dpp v116, v236 row_shr:2 row_mask:0xf bank_mask:0xf
	v_mov_b32_dpp v117, v237 row_shr:2 row_mask:0xf bank_mask:0xf
	v_mov_b32_e32 v112, v124
	v_mov_b32_e32 v113, v222
	v_mov_b32_e32 v114, v104
	v_mov_b32_e32 v115, v98
	v_mov_b32_dpp v136, v146 row_ror:1 row_mask:0xf bank_mask:0xf
	v_mov_b32_dpp v144, v146 row_ror:2 row_mask:0xf bank_mask:0xf
	v_mov_b32_dpp v232, v147 row_ror:1 row_mask:0xf bank_mask:0xf
	v_mov_b32_dpp v234, v147 row_ror:2 row_mask:0xf bank_mask:0xf
	v_mov_b32_dpp v118, v236 row_shr:1 row_mask:0xf bank_mask:0xf
	v_mov_b32_dpp v119, v237 row_shr:1 row_mask:0xf bank_mask:0xf
	v_pk_fma_f32 v[146:147], v[112:113], v[116:117], v[114:115]
	v_mov_b32_e32 v116, v120
	v_mov_b32_e32 v117, v224
	v_pk_fma_f32 v[146:147], v[116:117], v[118:119], v[146:147]
	v_mov_b32_e32 v118, v122
	v_mov_b32_e32 v119, v226
	v_pk_fma_f32 v[238:239], v[236:237], v[118:119], v[146:147]
	v_cvt_f32_i32_e32 v147, v23
	v_cvt_f32_i32_e32 v146, v47
	s_nop 0
	s_nop 0
	s_nop 0
	v_mov_b32_dpp v134, v145 row_ror:2 row_mask:0xf bank_mask:0xf
	v_mov_b32_dpp v133, v109 row_ror:1 row_mask:0xf bank_mask:0xf
	v_mov_b32_dpp v135, v109 row_ror:2 row_mask:0xf bank_mask:0xf
	v_pk_mul_f32 v[108:109], v[172:173], v[146:147] op_sel_hi:[0,1]
	s_nop 0
	v_mov_b32_e32 v222, v125
	v_mov_b32_dpp v134, v108 row_shr:2 row_mask:0xf bank_mask:0xf
	v_mov_b32_dpp v135, v109 row_shr:2 row_mask:0xf bank_mask:0xf
	v_mov_b32_e32 v98, v105
	v_mov_b32_dpp v132, v145 row_ror:1 row_mask:0xf bank_mask:0xf
	v_pk_fma_f32 v[104:105], v[222:223], v[134:135], v[98:99]
	v_mov_b32_e32 v224, v121
	v_cvt_f32_i32_e32 v121, v24
	v_cvt_f32_i32_e32 v120, v48
	v_cvt_f32_i32_e32 v135, v25
	v_cvt_f32_i32_e32 v134, v49
	v_mov_b32_dpp v132, v108 row_shr:1 row_mask:0xf bank_mask:0xf
	v_mov_b32_dpp v133, v109 row_shr:1 row_mask:0xf bank_mask:0xf
	v_pk_fma_f32 v[104:105], v[224:225], v[132:133], v[104:105]
	v_mov_b32_e32 v226, v123
	v_pk_fma_f32 v[104:105], v[108:109], v[226:227], v[104:105]
	s_nop 0
	s_nop 0
	s_nop 0
	s_nop 0
	v_mov_b32_dpp v137, v110 row_ror:1 row_mask:0xf bank_mask:0xf
	v_mov_b32_dpp v145, v110 row_ror:2 row_mask:0xf bank_mask:0xf
	v_pk_mul_f32 v[132:133], v[172:173], v[120:121] op_sel_hi:[0,1]
	v_mov_b32_e32 v121, v142
	v_mov_b32_dpp v233, v111 row_ror:1 row_mask:0xf bank_mask:0xf
	v_mov_b32_dpp v235, v111 row_ror:2 row_mask:0xf bank_mask:0xf
	v_pk_mul_f32 v[110:111], v[172:173], v[134:135] op_sel_hi:[0,1]
	v_mov_b32_e32 v142, v127
	v_mul_f32_e32 v127, 0xbfb8aa3b, v104
	v_mov_b32_dpp v144, v132 row_shr:2 row_mask:0xf bank_mask:0xf
	v_mov_b32_dpp v145, v133 row_shr:2 row_mask:0xf bank_mask:0xf
	v_mov_b32_e32 v120, v126
	v_mov_b32_e32 v122, v106
	v_mov_b32_e32 v123, v100
	v_mov_b32_dpp v234, v110 row_shr:2 row_mask:0xf bank_mask:0xf
	v_mov_b32_dpp v235, v111 row_shr:2 row_mask:0xf bank_mask:0xf
	v_mov_b32_e32 v100, v107
	v_exp_f32_e32 v127, v127
	v_mov_b32_dpp v136, v132 row_shr:1 row_mask:0xf bank_mask:0xf
	v_mov_b32_dpp v137, v133 row_shr:1 row_mask:0xf bank_mask:0xf
	v_pk_fma_f32 v[124:125], v[120:121], v[144:145], v[122:123]
	v_mov_b32_e32 v144, v128
	v_mov_b32_e32 v145, v220
	v_mov_b32_dpp v232, v110 row_shr:1 row_mask:0xf bank_mask:0xf
	v_mov_b32_dpp v233, v111 row_shr:1 row_mask:0xf bank_mask:0xf
	v_pk_fma_f32 v[106:107], v[142:143], v[234:235], v[100:101]
	v_mov_b32_e32 v220, v129
	v_pk_fma_f32 v[124:125], v[144:145], v[136:137], v[124:125]
	v_mov_b32_e32 v146, v130
	v_mov_b32_e32 v147, v140
	v_pk_fma_f32 v[106:107], v[220:221], v[232:233], v[106:107]
	v_mov_b32_e32 v140, v131
	v_pk_fma_f32 v[124:125], v[132:133], v[146:147], v[124:125]
	v_pk_fma_f32 v[106:107], v[110:111], v[140:141], v[106:107]
	v_add_f32_e32 v127, 1.0, v127
	v_mul_f32_e32 v128, 0xbfb8aa3b, v124
	v_mul_f32_e32 v129, 0xbfb8aa3b, v106
	v_mul_f32_e32 v126, 0xbfb8aa3b, v238
	v_rcp_f32_e32 v127, v127
	v_exp_f32_e32 v128, v128
	v_exp_f32_e32 v129, v129
	v_exp_f32_e32 v126, v126
	v_mul_f32_e32 v104, v104, v127
	v_add_f32_e32 v127, 1.0, v128
	v_add_f32_e32 v128, 1.0, v129
	v_add_f32_e32 v126, 1.0, v126
	v_rcp_f32_e32 v127, v127
	v_rcp_f32_e32 v128, v128
	v_rcp_f32_e32 v126, v126
	v_cvt_f32_i32_e32 v137, v18
	v_cvt_f32_i32_e32 v136, v42
	v_mul_f32_e32 v104, v104, v105
	v_mul_f32_e32 v105, v124, v127
	v_mul_f32_e32 v106, v106, v128
	v_lshl_add_u64 v[138:139], v[156:157], 1, s[8:9]
	v_mul_f32_e32 v126, v238, v126
	v_mul_f32_e32 v105, v105, v125
	v_mul_f32_e32 v106, v106, v107
	v_mul_f32_e32 v126, v126, v239
	v_cvt_pk_bf16_f32 v104, v126, v104
	v_cvt_pk_bf16_f32 v105, v105, v106
	v_mad_u64_u32 v[124:125], s[34:35], v169, s72, v[138:139]
	s_nop 0
	s_nop 0
	global_store_dwordx2 v[124:125], v[104:105], off
	s_nop 0
	v_mov_b32_dpp v106, v236 row_ror:2 row_mask:0xf bank_mask:0xf
	s_nop 0
	v_mov_b32_dpp v107, v237 row_ror:2 row_mask:0xf bank_mask:0xf
	v_pk_mul_f32 v[136:137], v[170:171], v[136:137] op_sel_hi:[0,1]
	v_mov_b32_dpp v104, v236 row_ror:1 row_mask:0xf bank_mask:0xf
	v_mov_b32_dpp v105, v237 row_ror:1 row_mask:0xf bank_mask:0xf
	v_mov_b32_dpp v106, v136 row_shr:2 row_mask:0xf bank_mask:0xf
	v_mov_b32_dpp v107, v137 row_shr:2 row_mask:0xf bank_mask:0xf
	v_mov_b32_dpp v104, v136 row_shr:1 row_mask:0xf bank_mask:0xf
	v_mov_b32_dpp v105, v137 row_shr:1 row_mask:0xf bank_mask:0xf
	v_pk_fma_f32 v[106:107], v[112:113], v[106:107], v[114:115]
	s_nop 0
	v_pk_fma_f32 v[104:105], v[116:117], v[104:105], v[106:107]
	v_cvt_f32_i32_e32 v107, v19
	v_cvt_f32_i32_e32 v106, v43
	s_nop 0
	s_nop 0
	v_mov_b32_dpp v128, v108 row_ror:2 row_mask:0xf bank_mask:0xf
	s_nop 0
	v_mov_b32_dpp v129, v109 row_ror:2 row_mask:0xf bank_mask:0xf
	v_pk_mul_f32 v[106:107], v[170:171], v[106:107] op_sel_hi:[0,1]
	v_mov_b32_dpp v126, v108 row_ror:1 row_mask:0xf bank_mask:0xf
	v_mov_b32_dpp v127, v109 row_ror:1 row_mask:0xf bank_mask:0xf
	v_mov_b32_dpp v128, v106 row_shr:2 row_mask:0xf bank_mask:0xf
	v_mov_b32_dpp v129, v107 row_shr:2 row_mask:0xf bank_mask:0xf
	v_mov_b32_dpp v126, v106 row_shr:1 row_mask:0xf bank_mask:0xf
	v_mov_b32_dpp v127, v107 row_shr:1 row_mask:0xf bank_mask:0xf
	v_pk_fma_f32 v[128:129], v[222:223], v[128:129], v[98:99]
	s_nop 0
	v_pk_fma_f32 v[126:127], v[224:225], v[126:127], v[128:129]
	v_cvt_f32_i32_e32 v129, v20
	v_cvt_f32_i32_e32 v128, v44
	s_nop 0
	s_nop 0
	v_mov_b32_dpp v130, v132 row_ror:2 row_mask:0xf bank_mask:0xf
	s_nop 0
	v_mov_b32_dpp v131, v133 row_ror:2 row_mask:0xf bank_mask:0xf
	v_pk_mul_f32 v[128:129], v[170:171], v[128:129] op_sel_hi:[0,1]
	v_mov_b32_dpp v108, v132 row_ror:1 row_mask:0xf bank_mask:0xf
	v_mov_b32_dpp v109, v133 row_ror:1 row_mask:0xf bank_mask:0xf
	v_mov_b32_dpp v130, v128 row_shr:2 row_mask:0xf bank_mask:0xf
	v_mov_b32_dpp v131, v129 row_shr:2 row_mask:0xf bank_mask:0xf
	v_mov_b32_dpp v108, v128 row_shr:1 row_mask:0xf bank_mask:0xf
	v_mov_b32_dpp v109, v129 row_shr:1 row_mask:0xf bank_mask:0xf
	v_pk_fma_f32 v[130:131], v[120:121], v[130:131], v[122:123]
	s_nop 0
	v_pk_fma_f32 v[108:109], v[144:145], v[108:109], v[130:131]
	v_cvt_f32_i32_e32 v131, v21
	v_cvt_f32_i32_e32 v130, v45
	s_nop 0
	v_pk_fma_f32 v[104:105], v[136:137], v[118:119], v[104:105]
	s_nop 0
	s_nop 0
	v_mov_b32_dpp v132, v110 row_ror:1 row_mask:0xf bank_mask:0xf
	v_mov_b32_dpp v134, v110 row_ror:2 row_mask:0xf bank_mask:0xf
	v_mov_b32_dpp v133, v111 row_ror:1 row_mask:0xf bank_mask:0xf
	v_mov_b32_dpp v135, v111 row_ror:2 row_mask:0xf bank_mask:0xf
	v_pk_mul_f32 v[110:111], v[170:171], v[130:131] op_sel_hi:[0,1]
	v_mul_f32_e32 v130, 0xbfb8aa3b, v104
	v_exp_f32_e32 v207, v130
	v_mov_b32_dpp v134, v110 row_shr:2 row_mask:0xf bank_mask:0xf
	v_mov_b32_dpp v135, v111 row_shr:2 row_mask:0xf bank_mask:0xf
	v_mov_b32_dpp v132, v110 row_shr:1 row_mask:0xf bank_mask:0xf
	v_mov_b32_dpp v133, v111 row_shr:1 row_mask:0xf bank_mask:0xf
	v_pk_fma_f32 v[130:131], v[142:143], v[134:135], v[100:101]
	v_pk_fma_f32 v[126:127], v[106:107], v[226:227], v[126:127]
	v_pk_fma_f32 v[130:131], v[220:221], v[132:133], v[130:131]
	v_add_f32_e32 v132, 1.0, v207
	v_rcp_f32_e32 v132, v132
	v_mul_f32_e32 v133, 0xbfb8aa3b, v126
	v_exp_f32_e32 v133, v133
	v_pk_fma_f32 v[108:109], v[128:129], v[146:147], v[108:109]
	v_mul_f32_e32 v104, v104, v132
	v_pk_fma_f32 v[130:131], v[110:111], v[140:141], v[130:131]
	v_mul_f32_e32 v104, v104, v105
	v_add_f32_e32 v105, 1.0, v133
	v_mul_f32_e32 v132, 0xbfb8aa3b, v108
	v_rcp_f32_e32 v105, v105
	v_exp_f32_e32 v132, v132
	v_mul_f32_e32 v133, 0xbfb8aa3b, v130
	v_exp_f32_e32 v133, v133
	v_mul_f32_e32 v105, v126, v105
	v_add_f32_e32 v126, 1.0, v132
	v_rcp_f32_e32 v126, v126
	v_add_f32_e32 v132, 1.0, v133
	v_rcp_f32_e32 v132, v132
	v_cvt_f32_i32_e32 v233, v14
	v_mul_f32_e32 v108, v108, v126
	v_cvt_f32_i32_e32 v232, v38
	v_mul_f32_e32 v105, v105, v127
	v_mul_f32_e32 v108, v108, v109
	v_mul_f32_e32 v109, v130, v132
	v_mul_f32_e32 v109, v109, v131
	v_cvt_pk_bf16_f32 v104, v104, v105
	v_cvt_pk_bf16_f32 v105, v108, v109
	v_add_u32_e32 v108, 16, v169
	v_mad_u64_u32 v[126:127], s[34:35], v108, s72, v[138:139]
	s_nop 0
	s_nop 0
	global_store_dwordx2 v[126:127], v[104:105], off
	s_nop 0
	v_mov_b32_dpp v108, v136 row_ror:2 row_mask:0xf bank_mask:0xf
	s_nop 0
	v_mov_b32_dpp v109, v137 row_ror:2 row_mask:0xf bank_mask:0xf
	v_pk_mul_f32 v[232:233], v[168:169], v[232:233] op_sel_hi:[0,1]
	v_mov_b32_dpp v104, v136 row_ror:1 row_mask:0xf bank_mask:0xf
	v_mov_b32_dpp v105, v137 row_ror:1 row_mask:0xf bank_mask:0xf
	v_mov_b32_dpp v108, v232 row_shr:2 row_mask:0xf bank_mask:0xf
	v_mov_b32_dpp v109, v233 row_shr:2 row_mask:0xf bank_mask:0xf
	v_mov_b32_dpp v104, v232 row_shr:1 row_mask:0xf bank_mask:0xf
	v_mov_b32_dpp v105, v233 row_shr:1 row_mask:0xf bank_mask:0xf
	v_pk_fma_f32 v[108:109], v[112:113], v[108:109], v[114:115]
	s_nop 0
	v_pk_fma_f32 v[104:105], v[116:117], v[104:105], v[108:109]
	v_cvt_f32_i32_e32 v109, v15
	v_cvt_f32_i32_e32 v108, v39
	s_nop 0
	s_nop 0
	v_mov_b32_dpp v132, v106 row_ror:2 row_mask:0xf bank_mask:0xf
	s_nop 0
	v_mov_b32_dpp v133, v107 row_ror:2 row_mask:0xf bank_mask:0xf
	v_pk_mul_f32 v[108:109], v[168:169], v[108:109] op_sel_hi:[0,1]
	v_mov_b32_dpp v130, v106 row_ror:1 row_mask:0xf bank_mask:0xf
	v_mov_b32_dpp v131, v107 row_ror:1 row_mask:0xf bank_mask:0xf
	v_mov_b32_dpp v132, v108 row_shr:2 row_mask:0xf bank_mask:0xf
	v_mov_b32_dpp v133, v109 row_shr:2 row_mask:0xf bank_mask:0xf
	v_mov_b32_dpp v130, v108 row_shr:1 row_mask:0xf bank_mask:0xf
	v_mov_b32_dpp v131, v109 row_shr:1 row_mask:0xf bank_mask:0xf
	v_pk_fma_f32 v[132:133], v[222:223], v[132:133], v[98:99]
	s_nop 0
	v_pk_fma_f32 v[130:131], v[224:225], v[130:131], v[132:133]
	v_cvt_f32_i32_e32 v133, v16
	v_cvt_f32_i32_e32 v132, v40
	s_nop 0
	s_nop 0
	v_mov_b32_dpp v134, v128 row_ror:2 row_mask:0xf bank_mask:0xf
	s_nop 0
	v_mov_b32_dpp v135, v129 row_ror:2 row_mask:0xf bank_mask:0xf
	v_pk_mul_f32 v[132:133], v[168:169], v[132:133] op_sel_hi:[0,1]
	v_mov_b32_dpp v106, v128 row_ror:1 row_mask:0xf bank_mask:0xf
	v_mov_b32_dpp v107, v129 row_ror:1 row_mask:0xf bank_mask:0xf
	v_mov_b32_dpp v134, v132 row_shr:2 row_mask:0xf bank_mask:0xf
	v_mov_b32_dpp v135, v133 row_shr:2 row_mask:0xf bank_mask:0xf
	v_mov_b32_dpp v106, v132 row_shr:1 row_mask:0xf bank_mask:0xf
	v_mov_b32_dpp v107, v133 row_shr:1 row_mask:0xf bank_mask:0xf
	v_pk_fma_f32 v[134:135], v[120:121], v[134:135], v[122:123]
	s_nop 0
	v_pk_fma_f32 v[106:107], v[144:145], v[106:107], v[134:135]
	v_cvt_f32_i32_e32 v135, v17
	v_cvt_f32_i32_e32 v134, v41
	s_nop 0
	v_pk_fma_f32 v[104:105], v[232:233], v[118:119], v[104:105]
	s_nop 0
	s_nop 0
	v_mov_b32_dpp v128, v110 row_ror:1 row_mask:0xf bank_mask:0xf
	v_mov_b32_dpp v136, v110 row_ror:2 row_mask:0xf bank_mask:0xf
	v_mov_b32_dpp v129, v111 row_ror:1 row_mask:0xf bank_mask:0xf
	v_mov_b32_dpp v137, v111 row_ror:2 row_mask:0xf bank_mask:0xf
	v_pk_mul_f32 v[110:111], v[168:169], v[134:135] op_sel_hi:[0,1]
	v_mul_f32_e32 v134, 0xbfb8aa3b, v104
	v_exp_f32_e32 v207, v134
	v_mov_b32_dpp v136, v110 row_shr:2 row_mask:0xf bank_mask:0xf
	v_mov_b32_dpp v137, v111 row_shr:2 row_mask:0xf bank_mask:0xf
	v_mov_b32_dpp v128, v110 row_shr:1 row_mask:0xf bank_mask:0xf
	v_mov_b32_dpp v129, v111 row_shr:1 row_mask:0xf bank_mask:0xf
	v_pk_fma_f32 v[134:135], v[142:143], v[136:137], v[100:101]
	v_pk_fma_f32 v[130:131], v[108:109], v[226:227], v[130:131]
	v_pk_fma_f32 v[128:129], v[220:221], v[128:129], v[134:135]
	v_add_f32_e32 v134, 1.0, v207
	v_rcp_f32_e32 v134, v134
	v_mul_f32_e32 v135, 0xbfb8aa3b, v130
	v_exp_f32_e32 v135, v135
	v_pk_fma_f32 v[106:107], v[132:133], v[146:147], v[106:107]
	v_mul_f32_e32 v104, v104, v134
	v_pk_fma_f32 v[128:129], v[110:111], v[140:141], v[128:129]
	v_mul_f32_e32 v104, v104, v105
	v_add_f32_e32 v105, 1.0, v135
	v_mul_f32_e32 v134, 0xbfb8aa3b, v106
	v_rcp_f32_e32 v105, v105
	v_exp_f32_e32 v134, v134
	v_mul_f32_e32 v135, 0xbfb8aa3b, v128
	v_exp_f32_e32 v135, v135
	v_mul_f32_e32 v105, v130, v105
	v_add_f32_e32 v130, 1.0, v134
	v_rcp_f32_e32 v130, v130
	v_add_f32_e32 v134, 1.0, v135
	v_rcp_f32_e32 v134, v134
	v_mul_f32_e32 v105, v105, v131
	v_mul_f32_e32 v106, v106, v130
	v_mul_f32_e32 v106, v106, v107
	v_mul_f32_e32 v107, v128, v134
	v_mul_f32_e32 v107, v107, v129
	v_cvt_pk_bf16_f32 v104, v104, v105
	v_cvt_pk_bf16_f32 v105, v106, v107
	v_add_u32_e32 v106, 32, v169
	v_mad_u64_u32 v[128:129], s[34:35], v106, s72, v[138:139]
	s_nop 0
	s_nop 0
	global_store_dwordx2 v[128:129], v[104:105], off
	s_nop 0
	v_mov_b32_dpp v106, v232 row_ror:2 row_mask:0xf bank_mask:0xf
	s_nop 0
	v_mov_b32_dpp v107, v233 row_ror:2 row_mask:0xf bank_mask:0xf
	v_pk_mul_f32 v[234:235], v[174:175], v[190:191] op_sel_hi:[0,1]
	v_mov_b32_dpp v104, v232 row_ror:1 row_mask:0xf bank_mask:0xf
	v_mov_b32_dpp v105, v233 row_ror:1 row_mask:0xf bank_mask:0xf
	v_mov_b32_dpp v106, v234 row_shr:2 row_mask:0xf bank_mask:0xf
	v_mov_b32_dpp v107, v235 row_shr:2 row_mask:0xf bank_mask:0xf
	s_nop 0
	v_mov_b32_dpp v104, v234 row_shr:1 row_mask:0xf bank_mask:0xf
	v_mov_b32_dpp v105, v235 row_shr:1 row_mask:0xf bank_mask:0xf
	v_pk_fma_f32 v[106:107], v[112:113], v[106:107], v[114:115]
	s_nop 0
	s_nop 0
	v_mov_b32_dpp v134, v108 row_ror:2 row_mask:0xf bank_mask:0xf
	v_pk_fma_f32 v[104:105], v[116:117], v[104:105], v[106:107]
	s_nop 0
	v_mov_b32_dpp v135, v109 row_ror:2 row_mask:0xf bank_mask:0xf
	v_pk_mul_f32 v[106:107], v[174:175], v[186:187] op_sel_hi:[0,1]
	v_mov_b32_dpp v130, v108 row_ror:1 row_mask:0xf bank_mask:0xf
	v_mov_b32_dpp v131, v109 row_ror:1 row_mask:0xf bank_mask:0xf
	v_mov_b32_dpp v134, v106 row_shr:2 row_mask:0xf bank_mask:0xf
	v_mov_b32_dpp v135, v107 row_shr:2 row_mask:0xf bank_mask:0xf
	v_mov_b32_dpp v130, v106 row_shr:1 row_mask:0xf bank_mask:0xf
	v_mov_b32_dpp v131, v107 row_shr:1 row_mask:0xf bank_mask:0xf
	v_pk_fma_f32 v[134:135], v[222:223], v[134:135], v[98:99]
	s_nop 0
	v_pk_fma_f32 v[130:131], v[224:225], v[130:131], v[134:135]
	s_nop 0
	s_nop 0
	v_mov_b32_dpp v136, v132 row_ror:2 row_mask:0xf bank_mask:0xf
	v_pk_fma_f32 v[106:107], v[106:107], v[226:227], v[130:131]
	s_nop 0
	v_mov_b32_dpp v137, v133 row_ror:2 row_mask:0xf bank_mask:0xf
	v_pk_mul_f32 v[130:131], v[174:175], v[188:189] op_sel_hi:[0,1]
	v_mov_b32_dpp v108, v132 row_ror:1 row_mask:0xf bank_mask:0xf
	v_mov_b32_dpp v109, v133 row_ror:1 row_mask:0xf bank_mask:0xf
	v_mov_b32_dpp v136, v130 row_shr:2 row_mask:0xf bank_mask:0xf
	v_mov_b32_dpp v137, v131 row_shr:2 row_mask:0xf bank_mask:0xf
	v_mov_b32_dpp v108, v130 row_shr:1 row_mask:0xf bank_mask:0xf
	v_mov_b32_dpp v109, v131 row_shr:1 row_mask:0xf bank_mask:0xf
	v_pk_fma_f32 v[134:135], v[120:121], v[136:137], v[122:123]
	v_pk_fma_f32 v[104:105], v[234:235], v[118:119], v[104:105]
	v_pk_fma_f32 v[108:109], v[144:145], v[108:109], v[134:135]
	s_nop 0
	v_pk_fma_f32 v[108:109], v[130:131], v[146:147], v[108:109]
	v_mul_f32_e32 v130, 0xbfb8aa3b, v104
	s_nop 0
	s_nop 0
	s_nop 0
	v_exp_f32_e32 v134, v130
	v_mov_b32_dpp v132, v110 row_ror:1 row_mask:0xf bank_mask:0xf
	v_mov_b32_dpp v232, v110 row_ror:2 row_mask:0xf bank_mask:0xf
	v_mov_b32_dpp v133, v111 row_ror:1 row_mask:0xf bank_mask:0xf
	v_mov_b32_dpp v233, v111 row_ror:2 row_mask:0xf bank_mask:0xf
	v_pk_mul_f32 v[110:111], v[174:175], v[184:185] op_sel_hi:[0,1]
	v_add_u32_e32 v103, s61, v103
	v_mov_b32_e32 v102, 0
	v_mov_b32_dpp v232, v110 row_shr:2 row_mask:0xf bank_mask:0xf
	v_mov_b32_dpp v233, v111 row_shr:2 row_mask:0xf bank_mask:0xf
	v_mov_b32_dpp v132, v110 row_shr:1 row_mask:0xf bank_mask:0xf
	v_mov_b32_dpp v133, v111 row_shr:1 row_mask:0xf bank_mask:0xf
	v_pk_fma_f32 v[130:131], v[142:143], v[232:233], v[100:101]
	v_lshl_add_u32 v195, v103, 9, v195
	v_pk_fma_f32 v[130:131], v[220:221], v[132:133], v[130:131]
	v_add_f32_e32 v132, 1.0, v134
	v_rcp_f32_e32 v132, v132
	v_mul_f32_e32 v133, 0xbfb8aa3b, v106
	v_exp_f32_e32 v133, v133
	v_pk_fma_f32 v[110:111], v[110:111], v[140:141], v[130:131]
	v_mul_f32_e32 v104, v104, v132
	v_mul_f32_e32 v104, v104, v105
	v_add_f32_e32 v105, 1.0, v133
	v_mul_f32_e32 v130, 0xbfb8aa3b, v108
	v_rcp_f32_e32 v105, v105
	v_exp_f32_e32 v130, v130
	v_mul_f32_e32 v131, 0xbfb8aa3b, v110
	v_exp_f32_e32 v131, v131
	v_mul_f32_e32 v105, v106, v105
	v_add_f32_e32 v106, 1.0, v130
	v_rcp_f32_e32 v106, v106
	v_add_f32_e32 v130, 1.0, v131
	v_rcp_f32_e32 v130, v130
	v_mul_f32_e32 v105, v105, v107
	v_mul_f32_e32 v106, v108, v106
	v_mul_f32_e32 v106, v106, v109
	v_mul_f32_e32 v107, v110, v130
	v_mul_f32_e32 v107, v107, v111
	v_cvt_pk_bf16_f32 v104, v104, v105
	v_cvt_pk_bf16_f32 v105, v106, v107
	v_add_u32_e32 v106, 48, v169
	v_mad_u64_u32 v[132:133], s[34:35], v106, s72, v[138:139]
	v_mov_b32_e32 v106, 0
	v_mov_b32_e32 v107, 0
	v_mov_b32_e32 v108, 0
	v_mov_b32_e32 v109, 0
	global_store_dwordx2 v[132:133], v[104:105], off
	s_and_saveexec_b64 s[34:35], vcc
	ds_read_b128 v[106:109], v195
	s_or_b64 exec, exec, s[34:35]
	v_mov_b32_e32 v103, 0
	v_mov_b32_e32 v104, 0
	v_mov_b32_e32 v105, 0
	s_and_saveexec_b64 s[34:35], vcc
	ds_read_b128 v[102:105], v195 offset:512
	s_or_b64 exec, exec, s[34:35]
	v_cvt_f32_i32_e32 v237, v90
	v_cvt_f32_i32_e32 v91, v91
	v_cvt_f32_i32_e32 v90, v95
	v_cvt_f32_i32_e32 v236, v94
	v_mov_b32_e32 v110, v157
	v_mov_b32_e32 v130, v157
	v_mov_b32_e32 v134, v157
	s_waitcnt lgkmcnt(0)
	v_mov_b32_dpp v110, v106 row_ror:1 row_mask:0xf bank_mask:0xf
	v_mov_b32_dpp v130, v106 row_ror:2 row_mask:0xf bank_mask:0xf
	v_mov_b32_e32 v106, v157
	v_mov_b32_e32 v135, v157
	v_mov_b32_dpp v134, v107 row_ror:2 row_mask:0xf bank_mask:0xf
	v_mov_b32_dpp v106, v107 row_ror:1 row_mask:0xf bank_mask:0xf
	v_mov_b32_e32 v111, v157
	v_mov_b32_e32 v131, v157
	v_mov_b32_e32 v107, v157
	v_mov_b32_dpp v135, v103 row_ror:2 row_mask:0xf bank_mask:0xf
	v_pk_mul_f32 v[90:91], v[208:209], v[90:91] op_sel_hi:[0,1]
	v_mov_b32_dpp v111, v102 row_ror:1 row_mask:0xf bank_mask:0xf
	v_mov_b32_dpp v131, v102 row_ror:2 row_mask:0xf bank_mask:0xf
	v_pk_mul_f32 v[236:237], v[208:209], v[236:237] op_sel_hi:[0,1]
	v_mov_b32_dpp v107, v103 row_ror:1 row_mask:0xf bank_mask:0xf
	v_mov_b32_dpp v134, v90 row_shr:2 row_mask:0xf bank_mask:0xf
	v_mov_b32_dpp v135, v91 row_shr:2 row_mask:0xf bank_mask:0xf
	v_cvt_f32_i32_e32 v103, v92
	v_cvt_f32_i32_e32 v102, v96
	v_cvt_f32_i32_e32 v93, v93
	v_cvt_f32_i32_e32 v92, v97
	v_mov_b32_e32 v136, v157
	v_mov_b32_e32 v232, v157
	v_mov_b32_dpp v130, v236 row_shr:2 row_mask:0xf bank_mask:0xf
	v_mov_b32_dpp v131, v237 row_shr:2 row_mask:0xf bank_mask:0xf
	v_mov_b32_dpp v106, v90 row_shr:1 row_mask:0xf bank_mask:0xf
	v_mov_b32_dpp v107, v91 row_shr:1 row_mask:0xf bank_mask:0xf
	v_pk_fma_f32 v[94:95], v[222:223], v[134:135], v[98:99]
	v_mov_b32_dpp v136, v108 row_ror:1 row_mask:0xf bank_mask:0xf
	v_mov_b32_dpp v232, v108 row_ror:2 row_mask:0xf bank_mask:0xf
	v_mov_b32_e32 v108, v157
	v_mov_b32_e32 v234, v157
	v_mov_b32_dpp v110, v236 row_shr:1 row_mask:0xf bank_mask:0xf
	v_mov_b32_dpp v111, v237 row_shr:1 row_mask:0xf bank_mask:0xf
	v_pk_fma_f32 v[130:131], v[112:113], v[130:131], v[114:115]
	v_pk_fma_f32 v[94:95], v[224:225], v[106:107], v[94:95]
	v_mov_b32_dpp v108, v109 row_ror:1 row_mask:0xf bank_mask:0xf
	v_mov_b32_dpp v234, v109 row_ror:2 row_mask:0xf bank_mask:0xf
	v_pk_fma_f32 v[110:111], v[116:117], v[110:111], v[130:131]
	v_pk_fma_f32 v[94:95], v[90:91], v[226:227], v[94:95]
	v_mov_b32_e32 v233, v157
	v_mov_b32_e32 v109, v157
	v_mov_b32_e32 v235, v157
	v_pk_fma_f32 v[110:111], v[236:237], v[118:119], v[110:111]
	v_mov_b32_e32 v137, v157
	v_mov_b32_dpp v233, v104 row_ror:2 row_mask:0xf bank_mask:0xf
	v_pk_mul_f32 v[102:103], v[208:209], v[102:103] op_sel_hi:[0,1]
	v_mov_b32_dpp v109, v105 row_ror:1 row_mask:0xf bank_mask:0xf
	v_mov_b32_dpp v235, v105 row_ror:2 row_mask:0xf bank_mask:0xf
	v_pk_mul_f32 v[92:93], v[208:209], v[92:93] op_sel_hi:[0,1]
	v_mul_f32_e32 v105, 0xbfb8aa3b, v94
	v_mov_b32_dpp v137, v104 row_ror:1 row_mask:0xf bank_mask:0xf
	v_mov_b32_dpp v232, v102 row_shr:2 row_mask:0xf bank_mask:0xf
	v_mov_b32_dpp v233, v103 row_shr:2 row_mask:0xf bank_mask:0xf
	v_mov_b32_dpp v234, v92 row_shr:2 row_mask:0xf bank_mask:0xf
	v_mul_f32_e32 v96, 0xbfb8aa3b, v110
	v_mov_b32_dpp v235, v93 row_shr:2 row_mask:0xf bank_mask:0xf
	v_exp_f32_e32 v105, v105
	v_mov_b32_dpp v136, v102 row_shr:1 row_mask:0xf bank_mask:0xf
	v_mov_b32_dpp v137, v103 row_shr:1 row_mask:0xf bank_mask:0xf
	v_pk_fma_f32 v[106:107], v[120:121], v[232:233], v[122:123]
	v_mov_b32_dpp v108, v92 row_shr:1 row_mask:0xf bank_mask:0xf
	v_mov_b32_dpp v109, v93 row_shr:1 row_mask:0xf bank_mask:0xf
	v_exp_f32_e32 v104, v96
	v_pk_fma_f32 v[96:97], v[142:143], v[234:235], v[100:101]
	v_pk_fma_f32 v[106:107], v[144:145], v[136:137], v[106:107]
	v_pk_fma_f32 v[96:97], v[220:221], v[108:109], v[96:97]
	v_pk_fma_f32 v[106:107], v[102:103], v[146:147], v[106:107]
	v_pk_fma_f32 v[96:97], v[92:93], v[140:141], v[96:97]
	v_add_f32_e32 v105, 1.0, v105
	v_mul_f32_e32 v108, 0xbfb8aa3b, v106
	v_mul_f32_e32 v109, 0xbfb8aa3b, v96
	v_rcp_f32_e32 v105, v105
	v_exp_f32_e32 v108, v108
	v_exp_f32_e32 v109, v109
	v_add_f32_e32 v104, 1.0, v104
	v_mul_f32_e32 v94, v94, v105
	v_add_f32_e32 v105, 1.0, v108
	v_add_f32_e32 v108, 1.0, v109
	v_rcp_f32_e32 v105, v105
	v_rcp_f32_e32 v108, v108
	v_rcp_f32_e32 v104, v104
	v_cvt_f32_i32_e32 v135, v82
	v_cvt_f32_i32_e32 v134, v86
	v_mul_f32_e32 v94, v94, v95
	v_mul_f32_e32 v95, v106, v105
	v_mul_f32_e32 v96, v96, v108
	v_add_u32_e32 v207, 0x80, v169
	v_mul_f32_e32 v104, v110, v104
	v_mul_f32_e32 v95, v95, v107
	v_mul_f32_e32 v96, v96, v97
	v_mul_f32_e32 v104, v104, v111
	v_cvt_pk_bf16_f32 v94, v104, v94
	v_cvt_pk_bf16_f32 v95, v95, v96
	v_mad_u64_u32 v[130:131], s[34:35], v207, s72, v[138:139]
	v_mov_b32_e32 v96, v157
	v_mov_b32_e32 v97, v157
	global_store_dwordx2 v[130:131], v[94:95], off
	v_mov_b32_e32 v94, v157
	v_mov_b32_dpp v96, v236 row_ror:2 row_mask:0xf bank_mask:0xf
	v_mov_b32_e32 v95, v157
	v_mov_b32_dpp v97, v237 row_ror:2 row_mask:0xf bank_mask:0xf
	v_pk_mul_f32 v[136:137], v[206:207], v[134:135] op_sel_hi:[0,1]
	v_mov_b32_dpp v94, v236 row_ror:1 row_mask:0xf bank_mask:0xf
	v_mov_b32_dpp v95, v237 row_ror:1 row_mask:0xf bank_mask:0xf
	v_mov_b32_dpp v96, v136 row_shr:2 row_mask:0xf bank_mask:0xf
	v_mov_b32_dpp v97, v137 row_shr:2 row_mask:0xf bank_mask:0xf
	v_mov_b32_dpp v94, v136 row_shr:1 row_mask:0xf bank_mask:0xf
	v_mov_b32_dpp v95, v137 row_shr:1 row_mask:0xf bank_mask:0xf
	v_pk_fma_f32 v[96:97], v[112:113], v[96:97], v[114:115]
	v_cvt_f32_i32_e32 v83, v83
	v_cvt_f32_i32_e32 v82, v87
	v_mov_b32_e32 v104, v157
	v_mov_b32_e32 v106, v157
	v_pk_fma_f32 v[94:95], v[116:117], v[94:95], v[96:97]
	v_mov_b32_dpp v104, v90 row_ror:1 row_mask:0xf bank_mask:0xf
	v_mov_b32_dpp v106, v90 row_ror:2 row_mask:0xf bank_mask:0xf
	v_mov_b32_e32 v90, v157
	v_mov_b32_e32 v108, v157
	v_pk_fma_f32 v[94:95], v[136:137], v[118:119], v[94:95]
	v_mov_b32_dpp v90, v102 row_ror:1 row_mask:0xf bank_mask:0xf
	v_mov_b32_dpp v108, v102 row_ror:2 row_mask:0xf bank_mask:0xf
	v_mov_b32_e32 v102, v157
	v_mov_b32_e32 v110, v157
	v_mov_b32_e32 v107, v157
	v_cvt_f32_i32_e32 v96, v88
	v_mul_f32_e32 v88, 0xbfb8aa3b, v94
	v_mov_b32_dpp v102, v92 row_ror:1 row_mask:0xf bank_mask:0xf
	v_mov_b32_dpp v110, v92 row_ror:2 row_mask:0xf bank_mask:0xf
	v_mov_b32_e32 v105, v157
	v_mov_b32_dpp v107, v91 row_ror:2 row_mask:0xf bank_mask:0xf
	v_pk_mul_f32 v[82:83], v[206:207], v[82:83] op_sel_hi:[0,1]
	v_exp_f32_e32 v92, v88
	v_mov_b32_dpp v105, v91 row_ror:1 row_mask:0xf bank_mask:0xf
	v_mov_b32_dpp v106, v82 row_shr:2 row_mask:0xf bank_mask:0xf
	v_mov_b32_dpp v107, v83 row_shr:2 row_mask:0xf bank_mask:0xf
	v_cvt_f32_i32_e32 v97, v84
	v_cvt_f32_i32_e32 v85, v85
	v_cvt_f32_i32_e32 v84, v89
	v_mov_b32_dpp v104, v82 row_shr:1 row_mask:0xf bank_mask:0xf
	v_mov_b32_dpp v105, v83 row_shr:1 row_mask:0xf bank_mask:0xf
	v_pk_fma_f32 v[86:87], v[222:223], v[106:107], v[98:99]
	v_mov_b32_e32 v91, v157
	v_pk_fma_f32 v[86:87], v[224:225], v[104:105], v[86:87]
	v_mov_b32_e32 v109, v157
	v_pk_fma_f32 v[86:87], v[82:83], v[226:227], v[86:87]
	v_mov_b32_dpp v91, v103 row_ror:1 row_mask:0xf bank_mask:0xf
	v_mov_b32_dpp v109, v103 row_ror:2 row_mask:0xf bank_mask:0xf
	v_mov_b32_e32 v103, v157
	v_mov_b32_e32 v111, v157
	v_add_f32_e32 v92, 1.0, v92
	v_pk_mul_f32 v[96:97], v[206:207], v[96:97] op_sel_hi:[0,1]
	v_mov_b32_dpp v103, v93 row_ror:1 row_mask:0xf bank_mask:0xf
	v_mov_b32_dpp v111, v93 row_ror:2 row_mask:0xf bank_mask:0xf
	v_pk_mul_f32 v[84:85], v[206:207], v[84:85] op_sel_hi:[0,1]
	v_rcp_f32_e32 v92, v92
	v_mul_f32_e32 v93, 0xbfb8aa3b, v86
	v_mov_b32_dpp v108, v96 row_shr:2 row_mask:0xf bank_mask:0xf
	v_mov_b32_dpp v109, v97 row_shr:2 row_mask:0xf bank_mask:0xf
	v_mov_b32_dpp v110, v84 row_shr:2 row_mask:0xf bank_mask:0xf
	v_mov_b32_dpp v111, v85 row_shr:2 row_mask:0xf bank_mask:0xf
	v_exp_f32_e32 v93, v93
	v_mov_b32_dpp v90, v96 row_shr:1 row_mask:0xf bank_mask:0xf
	v_mov_b32_dpp v91, v97 row_shr:1 row_mask:0xf bank_mask:0xf
	v_pk_fma_f32 v[104:105], v[120:121], v[108:109], v[122:123]
	v_mov_b32_dpp v102, v84 row_shr:1 row_mask:0xf bank_mask:0xf
	v_mov_b32_dpp v103, v85 row_shr:1 row_mask:0xf bank_mask:0xf
	v_pk_fma_f32 v[88:89], v[142:143], v[110:111], v[100:101]
	v_pk_fma_f32 v[90:91], v[144:145], v[90:91], v[104:105]
	v_pk_fma_f32 v[88:89], v[220:221], v[102:103], v[88:89]
	v_pk_fma_f32 v[90:91], v[96:97], v[146:147], v[90:91]
	v_pk_fma_f32 v[88:89], v[84:85], v[140:141], v[88:89]
	v_mul_f32_e32 v92, v94, v92
	v_mul_f32_e32 v92, v92, v95
	v_add_f32_e32 v93, 1.0, v93
	v_mul_f32_e32 v94, 0xbfb8aa3b, v90
	v_mul_f32_e32 v95, 0xbfb8aa3b, v88
	v_rcp_f32_e32 v93, v93
	v_exp_f32_e32 v94, v94
	v_exp_f32_e32 v95, v95
	v_cvt_f32_i32_e32 v105, v74
	v_mul_f32_e32 v86, v86, v93
	v_add_f32_e32 v93, 1.0, v94
	v_add_f32_e32 v94, 1.0, v95
	v_rcp_f32_e32 v93, v93
	v_rcp_f32_e32 v94, v94
	v_mul_f32_e32 v86, v86, v87
	v_cvt_f32_i32_e32 v104, v78
	v_mul_f32_e32 v87, v90, v93
	v_mul_f32_e32 v88, v88, v94
	v_mul_f32_e32 v87, v87, v91
	v_mul_f32_e32 v88, v88, v89
	v_cvt_pk_bf16_f32 v86, v92, v86
	v_cvt_pk_bf16_f32 v87, v87, v88
	v_add_u32_e32 v88, 0x90, v169
	v_mad_u64_u32 v[134:135], s[34:35], v88, s72, v[138:139]
	v_mov_b32_e32 v88, v157
	v_mov_b32_e32 v89, v157
	global_store_dwordx2 v[134:135], v[86:87], off
	v_mov_b32_e32 v86, v157
	v_mov_b32_dpp v88, v136 row_ror:2 row_mask:0xf bank_mask:0xf
	v_mov_b32_e32 v87, v157
	v_mov_b32_dpp v89, v137 row_ror:2 row_mask:0xf bank_mask:0xf
	v_pk_mul_f32 v[104:105], v[198:199], v[104:105] op_sel_hi:[0,1]
	v_mov_b32_dpp v86, v136 row_ror:1 row_mask:0xf bank_mask:0xf
	v_mov_b32_dpp v87, v137 row_ror:1 row_mask:0xf bank_mask:0xf
	v_mov_b32_dpp v88, v104 row_shr:2 row_mask:0xf bank_mask:0xf
	v_mov_b32_dpp v89, v105 row_shr:2 row_mask:0xf bank_mask:0xf
	v_mov_b32_dpp v86, v104 row_shr:1 row_mask:0xf bank_mask:0xf
	v_mov_b32_dpp v87, v105 row_shr:1 row_mask:0xf bank_mask:0xf
	v_pk_fma_f32 v[88:89], v[112:113], v[88:89], v[114:115]
	v_cvt_f32_i32_e32 v75, v75
	v_cvt_f32_i32_e32 v74, v79
	v_mov_b32_e32 v90, v157
	v_mov_b32_e32 v92, v157
	v_pk_fma_f32 v[86:87], v[116:117], v[86:87], v[88:89]
	v_mov_b32_dpp v90, v82 row_ror:1 row_mask:0xf bank_mask:0xf
	v_mov_b32_dpp v92, v82 row_ror:2 row_mask:0xf bank_mask:0xf
	v_mov_b32_e32 v82, v157
	v_mov_b32_e32 v94, v157
	v_pk_fma_f32 v[86:87], v[104:105], v[118:119], v[86:87]
	v_mov_b32_dpp v82, v96 row_ror:1 row_mask:0xf bank_mask:0xf
	v_mov_b32_dpp v94, v96 row_ror:2 row_mask:0xf bank_mask:0xf
	v_mov_b32_e32 v96, v157
	v_mov_b32_e32 v102, v157
	v_mov_b32_e32 v93, v157
	v_cvt_f32_i32_e32 v88, v80
	v_mul_f32_e32 v80, 0xbfb8aa3b, v86
	v_mov_b32_dpp v96, v84 row_ror:1 row_mask:0xf bank_mask:0xf
	v_mov_b32_dpp v102, v84 row_ror:2 row_mask:0xf bank_mask:0xf
	v_mov_b32_e32 v91, v157
	v_mov_b32_dpp v93, v83 row_ror:2 row_mask:0xf bank_mask:0xf
	v_pk_mul_f32 v[74:75], v[198:199], v[74:75] op_sel_hi:[0,1]
	v_exp_f32_e32 v84, v80
	v_mov_b32_dpp v91, v83 row_ror:1 row_mask:0xf bank_mask:0xf
	v_mov_b32_dpp v92, v74 row_shr:2 row_mask:0xf bank_mask:0xf
	v_mov_b32_dpp v93, v75 row_shr:2 row_mask:0xf bank_mask:0xf
	v_cvt_f32_i32_e32 v89, v76
	v_cvt_f32_i32_e32 v77, v77
	v_cvt_f32_i32_e32 v76, v81
	v_mov_b32_dpp v90, v74 row_shr:1 row_mask:0xf bank_mask:0xf
	v_mov_b32_dpp v91, v75 row_shr:1 row_mask:0xf bank_mask:0xf
	v_pk_fma_f32 v[78:79], v[222:223], v[92:93], v[98:99]
	v_mov_b32_e32 v83, v157
	v_pk_fma_f32 v[78:79], v[224:225], v[90:91], v[78:79]
	v_mov_b32_e32 v95, v157
	v_pk_fma_f32 v[78:79], v[74:75], v[226:227], v[78:79]
	v_mov_b32_dpp v83, v97 row_ror:1 row_mask:0xf bank_mask:0xf
	v_mov_b32_dpp v95, v97 row_ror:2 row_mask:0xf bank_mask:0xf
	v_mov_b32_e32 v97, v157
	v_mov_b32_e32 v103, v157
	v_add_f32_e32 v84, 1.0, v84
	v_pk_mul_f32 v[88:89], v[198:199], v[88:89] op_sel_hi:[0,1]
	v_mov_b32_dpp v97, v85 row_ror:1 row_mask:0xf bank_mask:0xf
	v_mov_b32_dpp v103, v85 row_ror:2 row_mask:0xf bank_mask:0xf
	v_pk_mul_f32 v[76:77], v[198:199], v[76:77] op_sel_hi:[0,1]
	v_rcp_f32_e32 v84, v84
	v_mul_f32_e32 v85, 0xbfb8aa3b, v78
	v_mov_b32_dpp v94, v88 row_shr:2 row_mask:0xf bank_mask:0xf
	v_mov_b32_dpp v95, v89 row_shr:2 row_mask:0xf bank_mask:0xf
	v_mov_b32_dpp v102, v76 row_shr:2 row_mask:0xf bank_mask:0xf
	v_mov_b32_dpp v103, v77 row_shr:2 row_mask:0xf bank_mask:0xf
	v_exp_f32_e32 v85, v85
	v_mov_b32_dpp v82, v88 row_shr:1 row_mask:0xf bank_mask:0xf
	v_mov_b32_dpp v83, v89 row_shr:1 row_mask:0xf bank_mask:0xf
	v_pk_fma_f32 v[90:91], v[120:121], v[94:95], v[122:123]
	v_mov_b32_dpp v96, v76 row_shr:1 row_mask:0xf bank_mask:0xf
	v_mov_b32_dpp v97, v77 row_shr:1 row_mask:0xf bank_mask:0xf
	v_pk_fma_f32 v[80:81], v[142:143], v[102:103], v[100:101]
	v_pk_fma_f32 v[82:83], v[144:145], v[82:83], v[90:91]
	v_pk_fma_f32 v[80:81], v[220:221], v[96:97], v[80:81]
	v_pk_fma_f32 v[82:83], v[88:89], v[146:147], v[82:83]
	v_pk_fma_f32 v[80:81], v[76:77], v[140:141], v[80:81]
	v_mul_f32_e32 v84, v86, v84
	v_mul_f32_e32 v84, v84, v87
	v_add_f32_e32 v85, 1.0, v85
	v_mul_f32_e32 v86, 0xbfb8aa3b, v82
	v_mul_f32_e32 v87, 0xbfb8aa3b, v80
	v_rcp_f32_e32 v85, v85
	v_exp_f32_e32 v86, v86
	v_exp_f32_e32 v87, v87
	v_pk_mul_f32 v[92:93], v[194:195], v[218:219] op_sel_hi:[0,1]
	v_mul_f32_e32 v78, v78, v85
	v_add_f32_e32 v85, 1.0, v86
	v_add_f32_e32 v86, 1.0, v87
	v_rcp_f32_e32 v85, v85
	v_rcp_f32_e32 v86, v86
	v_mul_f32_e32 v78, v78, v79
	v_cvt_pk_bf16_f32 v78, v84, v78
	v_mul_f32_e32 v79, v82, v85
	v_mul_f32_e32 v80, v80, v86
	v_mul_f32_e32 v79, v79, v83
	v_mul_f32_e32 v80, v80, v81
	v_cvt_pk_bf16_f32 v79, v79, v80
	v_add_u32_e32 v80, 0xa0, v169
	v_mad_u64_u32 v[136:137], s[34:35], v80, s72, v[138:139]
	v_mov_b32_e32 v80, v157
	v_mov_b32_e32 v81, v157
	global_store_dwordx2 v[136:137], v[78:79], off
	v_mov_b32_e32 v78, v157
	v_mov_b32_dpp v80, v104 row_ror:2 row_mask:0xf bank_mask:0xf
	v_mov_b32_e32 v79, v157
	v_mov_b32_dpp v81, v105 row_ror:2 row_mask:0xf bank_mask:0xf
	v_mov_b32_dpp v78, v104 row_ror:1 row_mask:0xf bank_mask:0xf
	v_mov_b32_dpp v79, v105 row_ror:1 row_mask:0xf bank_mask:0xf
	v_mov_b32_dpp v80, v92 row_shr:2 row_mask:0xf bank_mask:0xf
	v_mov_b32_dpp v81, v93 row_shr:2 row_mask:0xf bank_mask:0xf
	v_mov_b32_e32 v84, v157
	v_mov_b32_dpp v78, v92 row_shr:1 row_mask:0xf bank_mask:0xf
	v_mov_b32_dpp v79, v93 row_shr:1 row_mask:0xf bank_mask:0xf
	v_pk_fma_f32 v[80:81], v[112:113], v[80:81], v[114:115]
	v_mov_b32_e32 v85, v157
	v_mov_b32_e32 v82, v157
	v_mov_b32_dpp v84, v74 row_ror:2 row_mask:0xf bank_mask:0xf
	v_pk_fma_f32 v[78:79], v[116:117], v[78:79], v[80:81]
	v_mov_b32_e32 v83, v157
	v_mov_b32_dpp v85, v75 row_ror:2 row_mask:0xf bank_mask:0xf
	v_pk_mul_f32 v[80:81], v[194:195], v[216:217] op_sel_hi:[0,1]
	v_mov_b32_dpp v82, v74 row_ror:1 row_mask:0xf bank_mask:0xf
	v_mov_b32_dpp v83, v75 row_ror:1 row_mask:0xf bank_mask:0xf
	v_mov_b32_dpp v84, v80 row_shr:2 row_mask:0xf bank_mask:0xf
	v_mov_b32_dpp v85, v81 row_shr:2 row_mask:0xf bank_mask:0xf
	v_mov_b32_dpp v82, v80 row_shr:1 row_mask:0xf bank_mask:0xf
	v_mov_b32_dpp v83, v81 row_shr:1 row_mask:0xf bank_mask:0xf
	v_pk_fma_f32 v[84:85], v[222:223], v[84:85], v[98:99]
	v_mov_b32_e32 v86, v157
	v_pk_fma_f32 v[82:83], v[224:225], v[82:83], v[84:85]
	v_mov_b32_e32 v87, v157
	v_mov_b32_e32 v74, v157
	v_mov_b32_dpp v86, v88 row_ror:2 row_mask:0xf bank_mask:0xf
	v_pk_fma_f32 v[80:81], v[80:81], v[226:227], v[82:83]
	v_mov_b32_e32 v75, v157
	v_mov_b32_dpp v87, v89 row_ror:2 row_mask:0xf bank_mask:0xf
	v_pk_mul_f32 v[82:83], v[194:195], v[214:215] op_sel_hi:[0,1]
	v_mov_b32_dpp v74, v88 row_ror:1 row_mask:0xf bank_mask:0xf
	v_mov_b32_dpp v75, v89 row_ror:1 row_mask:0xf bank_mask:0xf
	v_mov_b32_dpp v86, v82 row_shr:2 row_mask:0xf bank_mask:0xf
	v_mov_b32_dpp v87, v83 row_shr:2 row_mask:0xf bank_mask:0xf
	v_mov_b32_dpp v74, v82 row_shr:1 row_mask:0xf bank_mask:0xf
	v_mov_b32_dpp v75, v83 row_shr:1 row_mask:0xf bank_mask:0xf
	v_pk_fma_f32 v[84:85], v[120:121], v[86:87], v[122:123]
	v_pk_fma_f32 v[78:79], v[92:93], v[118:119], v[78:79]
	v_pk_fma_f32 v[74:75], v[144:145], v[74:75], v[84:85]
	v_mov_b32_e32 v88, v157
	v_pk_fma_f32 v[74:75], v[82:83], v[146:147], v[74:75]
	v_mul_f32_e32 v82, 0xbfb8aa3b, v78
	v_exp_f32_e32 v84, v82
	v_mov_b32_e32 v90, v157
	v_mov_b32_e32 v89, v157
	v_mov_b32_e32 v91, v157
	v_add_f32_e32 v84, 1.0, v84
	v_rcp_f32_e32 v84, v84
	v_mul_f32_e32 v85, 0xbfb8aa3b, v80
	v_mov_b32_dpp v88, v76 row_ror:1 row_mask:0xf bank_mask:0xf
	v_mov_b32_dpp v90, v76 row_ror:2 row_mask:0xf bank_mask:0xf
	v_mov_b32_dpp v89, v77 row_ror:1 row_mask:0xf bank_mask:0xf
	v_mov_b32_dpp v91, v77 row_ror:2 row_mask:0xf bank_mask:0xf
	v_pk_mul_f32 v[76:77], v[194:195], v[210:211] op_sel_hi:[0,1]
	v_exp_f32_e32 v85, v85
	v_mul_f32_e32 v78, v78, v84
	v_mov_b32_dpp v90, v76 row_shr:2 row_mask:0xf bank_mask:0xf
	v_mov_b32_dpp v91, v77 row_shr:2 row_mask:0xf bank_mask:0xf
	v_mov_b32_dpp v88, v76 row_shr:1 row_mask:0xf bank_mask:0xf
	v_mov_b32_dpp v89, v77 row_shr:1 row_mask:0xf bank_mask:0xf
	v_pk_fma_f32 v[82:83], v[142:143], v[90:91], v[100:101]
	v_mul_f32_e32 v78, v78, v79
	v_pk_fma_f32 v[82:83], v[220:221], v[88:89], v[82:83]
	v_add_f32_e32 v79, 1.0, v85
	v_pk_fma_f32 v[76:77], v[76:77], v[140:141], v[82:83]
	v_mul_f32_e32 v82, 0xbfb8aa3b, v74
	v_rcp_f32_e32 v79, v79
	v_exp_f32_e32 v82, v82
	v_mul_f32_e32 v83, 0xbfb8aa3b, v76
	v_exp_f32_e32 v83, v83
	v_mul_f32_e32 v79, v80, v79
	v_add_f32_e32 v80, 1.0, v82
	v_rcp_f32_e32 v80, v80
	v_add_f32_e32 v82, 1.0, v83
	v_rcp_f32_e32 v82, v82
	v_mul_f32_e32 v79, v79, v81
	v_mul_f32_e32 v74, v74, v80
	v_mul_f32_e32 v74, v74, v75
	v_mul_f32_e32 v75, v76, v82
	v_mul_f32_e32 v75, v75, v77
	v_cvt_pk_bf16_f32 v76, v78, v79
	v_cvt_pk_bf16_f32 v77, v74, v75
	v_or_b32_e32 v74, 1, v199
	v_lshl_add_u32 v74, v74, 4, 0
	v_add_u32_e32 v75, 0x22400, v74
	v_add_u32_e32 v78, 0x22000, v74
	ds_read_b128 v[88:91], v75
	ds_read_b128 v[80:83], v78
	ds_read_b128 v[100:103], v78 offset:2048
	ds_read_b128 v[96:99], v78 offset:3072
	ds_read_b128 v[92:95], v78 offset:4096
	v_add_u32_e32 v75, 0xb0, v169
	v_mad_u64_u32 v[138:139], s[34:35], v75, s72, v[138:139]
	global_store_dwordx2 v[138:139], v[76:77], off
	s_and_saveexec_b64 s[34:35], s[0:1]
	s_cbranch_execz .LBB0_1679
	v_cvt_f32_i32_e32 v77, v37
	v_cvt_f32_i32_e32 v85, v35
	v_cvt_f32_i32_e32 v84, v34
	v_cvt_f32_i32_e32 v76, v36
	v_pk_mul_f32 v[84:85], v[172:173], v[84:85] op_sel_hi:[0,1]
	v_pk_mul_f32 v[76:77], v[172:173], v[76:77] op_sel_hi:[0,1]
	s_waitcnt lgkmcnt(4)
	v_pk_mul_f32 v[86:87], v[76:77], v[90:91]
	v_pk_mul_f32 v[84:85], v[84:85], v[88:89]
	v_mad_i64_i32 v[76:77], s[38:39], v173, s73, v[212:213]
	global_store_dwordx4 v[76:77], v[84:87], off offset:16

.LBB0_1691:
	s_and_b64 vcc, exec, s[0:1]
	s_cbranch_vccz .LBB0_1690
	v_or_b32_e32 v50, s55, v193
	v_mov_b32_e32 v193, v157
	v_lshlrev_b32_e32 v74, 1, v50
	v_lshl_add_u64 v[50:51], v[192:193], 2, s[22:23]
	global_load_dwordx4 v[54:57], v[50:51], off
	v_cvt_f32_i32_e32 v49, v49
	v_cvt_f32_i32_e32 v48, v48
	v_cvt_f32_i32_e32 v47, v47
	v_cvt_f32_i32_e32 v46, v46
	v_cvt_f32_i32_e32 v45, v45
	v_cvt_f32_i32_e32 v44, v44
	v_cvt_f32_i32_e32 v43, v43
	v_cvt_f32_i32_e32 v42, v42
	v_cvt_f32_i32_e32 v41, v41
	v_cvt_f32_i32_e32 v40, v40
	v_cvt_f32_i32_e32 v39, v39
	v_cvt_f32_i32_e32 v38, v38
	v_lshl_add_u64 v[52:53], v[156:157], 2, s[4:5]
	v_mov_b32_e32 v58, v190
	v_mov_b32_e32 v59, v186
	v_mov_b32_e32 v60, v188
	v_mov_b32_e32 v61, v184
	s_waitcnt vmcnt(0)
	v_pk_mul_f32 v[46:47], v[172:173], v[46:47] op_sel_hi:[0,1]
	v_pk_mul_f32 v[48:49], v[172:173], v[48:49] op_sel_hi:[0,1]
	v_pk_mul_f32 v[58:59], v[174:175], v[58:59] op_sel_hi:[0,1]
	v_pk_mul_f32 v[60:61], v[174:175], v[60:61] op_sel_hi:[0,1]
	v_mad_u64_u32 v[62:63], s[0:1], v74, s73, v[52:53]
	v_add_u32_e32 v64, 32, v74
	v_add_u32_e32 v70, 64, v74
	v_add_u32_e32 v72, 0x60, v74
	v_pk_mul_f32 v[42:43], v[170:171], v[42:43] op_sel_hi:[0,1]
	v_pk_mul_f32 v[44:45], v[170:171], v[44:45] op_sel_hi:[0,1]
	v_pk_mul_f32 v[66:67], v[168:169], v[38:39] op_sel_hi:[0,1]
	v_pk_mul_f32 v[68:69], v[168:169], v[40:41] op_sel_hi:[0,1]
	v_mad_u64_u32 v[64:65], s[0:1], v64, s73, v[52:53]
	v_mad_u64_u32 v[70:71], s[0:1], v70, s73, v[52:53]
	v_mad_u64_u32 v[72:73], s[0:1], v72, s73, v[52:53]
	v_cvt_f32_i32_e32 v37, v37
	v_cvt_f32_i32_e32 v36, v36
	v_cvt_f32_i32_e32 v35, v35
	v_cvt_f32_i32_e32 v34, v34
	v_cvt_f32_i32_e32 v33, v33
	v_cvt_f32_i32_e32 v32, v32
	v_cvt_f32_i32_e32 v31, v31
	v_cvt_f32_i32_e32 v30, v30
	v_cvt_f32_i32_e32 v29, v29
	v_cvt_f32_i32_e32 v28, v28
	v_cvt_f32_i32_e32 v27, v27
	v_cvt_f32_i32_e32 v26, v26
	v_pk_mul_f32 v[34:35], v[172:173], v[34:35] op_sel_hi:[0,1]
	v_pk_mul_f32 v[36:37], v[172:173], v[36:37] op_sel_hi:[0,1]
	v_pk_mul_f32 v[30:31], v[170:171], v[30:31] op_sel_hi:[0,1]
	v_pk_mul_f32 v[32:33], v[170:171], v[32:33] op_sel_hi:[0,1]
	v_cvt_f32_i32_e32 v25, v25
	v_cvt_f32_i32_e32 v24, v24
	v_cvt_f32_i32_e32 v23, v23
	v_cvt_f32_i32_e32 v22, v22
	v_cvt_f32_i32_e32 v21, v21
	v_cvt_f32_i32_e32 v20, v20
	v_cvt_f32_i32_e32 v19, v19
	v_cvt_f32_i32_e32 v18, v18
	v_cvt_f32_i32_e32 v17, v17
	v_cvt_f32_i32_e32 v16, v16
	v_cvt_f32_i32_e32 v15, v15
	v_cvt_f32_i32_e32 v14, v14
	v_mov_b32_e32 v186, v191
	v_mov_b32_e32 v184, v189
	v_pk_mul_f32 v[22:23], v[172:173], v[22:23] op_sel_hi:[0,1]
	v_pk_mul_f32 v[24:25], v[172:173], v[24:25] op_sel_hi:[0,1]
	v_pk_mul_f32 v[18:19], v[170:171], v[18:19] op_sel_hi:[0,1]
	v_pk_mul_f32 v[20:21], v[170:171], v[20:21] op_sel_hi:[0,1]
	v_cvt_f32_i32_e32 v13, v13
	v_cvt_f32_i32_e32 v12, v12
	v_cvt_f32_i32_e32 v11, v11
	v_cvt_f32_i32_e32 v10, v10
	v_cvt_f32_i32_e32 v9, v9
	v_cvt_f32_i32_e32 v8, v8
	v_cvt_f32_i32_e32 v7, v7
	v_cvt_f32_i32_e32 v6, v6
	v_cvt_f32_i32_e32 v5, v5
	v_pk_mul_f32 v[40:41], v[48:49], v[56:57]
	v_pk_mul_f32 v[38:39], v[46:47], v[54:55]
	v_pk_mul_f32 v[44:45], v[44:45], v[56:57]
	v_pk_mul_f32 v[42:43], v[42:43], v[54:55]
	v_pk_mul_f32 v[48:49], v[68:69], v[56:57]
	v_pk_mul_f32 v[46:47], v[66:67], v[54:55]
	v_pk_mul_f32 v[56:57], v[60:61], v[56:57]
	v_pk_mul_f32 v[54:55], v[58:59], v[54:55]
	global_store_dwordx4 v[62:63], v[38:41], off
	global_store_dwordx4 v[64:65], v[42:45], off
	global_store_dwordx4 v[70:71], v[46:49], off
	global_store_dwordx4 v[72:73], v[54:57], off
	global_load_dwordx4 v[38:41], v[50:51], off offset:16
	v_mov_b32_e32 v42, v182
	v_mov_b32_e32 v43, v178
	v_mov_b32_e32 v44, v180
	v_mov_b32_e32 v45, v176
	v_pk_mul_f32 v[42:43], v[174:175], v[42:43] op_sel_hi:[0,1]
	v_pk_mul_f32 v[44:45], v[174:175], v[44:45] op_sel_hi:[0,1]
	v_pk_mul_f32 v[46:47], v[168:169], v[26:27] op_sel_hi:[0,1]
	v_pk_mul_f32 v[48:49], v[168:169], v[28:29] op_sel_hi:[0,1]
	v_cvt_f32_i32_e32 v4, v4
	v_cvt_f32_i32_e32 v3, v3
	v_cvt_f32_i32_e32 v2, v2
	v_mov_b32_e32 v178, v183
	v_mov_b32_e32 v176, v181
	v_pk_mul_f32 v[10:11], v[172:173], v[10:11] op_sel_hi:[0,1]
	v_pk_mul_f32 v[12:13], v[172:173], v[12:13] op_sel_hi:[0,1]
	v_pk_mul_f32 v[6:7], v[170:171], v[6:7] op_sel_hi:[0,1]
	v_pk_mul_f32 v[8:9], v[170:171], v[8:9] op_sel_hi:[0,1]
	s_waitcnt vmcnt(0)
	v_pk_mul_f32 v[28:29], v[36:37], v[40:41]
	v_pk_mul_f32 v[26:27], v[34:35], v[38:39]
	v_pk_mul_f32 v[32:33], v[32:33], v[40:41]
	v_pk_mul_f32 v[30:31], v[30:31], v[38:39]
	v_pk_mul_f32 v[36:37], v[48:49], v[40:41]
	v_pk_mul_f32 v[34:35], v[46:47], v[38:39]
	v_pk_mul_f32 v[40:41], v[44:45], v[40:41]
	v_pk_mul_f32 v[38:39], v[42:43], v[38:39]
	global_store_dwordx4 v[62:63], v[26:29], off offset:16
	global_store_dwordx4 v[64:65], v[30:33], off offset:16
	global_store_dwordx4 v[70:71], v[34:37], off offset:16
	global_store_dwordx4 v[72:73], v[38:41], off offset:16
	global_load_dwordx4 v[26:29], v[50:51], off offset:512
	v_add_u32_e32 v34, 1, v74
	v_pk_mul_f32 v[30:31], v[174:175], v[186:187] op_sel_hi:[0,1]
	v_pk_mul_f32 v[32:33], v[174:175], v[184:185] op_sel_hi:[0,1]
	v_add_u32_e32 v36, 33, v74
	v_add_u32_e32 v42, 0x41, v74
	v_add_u32_e32 v44, 0x61, v74
	v_mad_u64_u32 v[34:35], s[0:1], v34, s73, v[52:53]
	v_pk_mul_f32 v[38:39], v[168:169], v[14:15] op_sel_hi:[0,1]
	v_pk_mul_f32 v[40:41], v[168:169], v[16:17] op_sel_hi:[0,1]
	v_mad_u64_u32 v[36:37], s[0:1], v36, s73, v[52:53]
	v_mad_u64_u32 v[42:43], s[0:1], v42, s73, v[52:53]
	v_mad_u64_u32 v[44:45], s[0:1], v44, s73, v[52:53]
	s_waitcnt vmcnt(0)
	v_pk_mul_f32 v[16:17], v[24:25], v[28:29]
	v_pk_mul_f32 v[14:15], v[22:23], v[26:27]
	v_pk_mul_f32 v[20:21], v[20:21], v[28:29]
	v_pk_mul_f32 v[18:19], v[18:19], v[26:27]
	v_pk_mul_f32 v[24:25], v[40:41], v[28:29]
	v_pk_mul_f32 v[22:23], v[38:39], v[26:27]
	v_pk_mul_f32 v[28:29], v[32:33], v[28:29]
	v_pk_mul_f32 v[26:27], v[30:31], v[26:27]
	global_store_dwordx4 v[34:35], v[14:17], off
	global_store_dwordx4 v[36:37], v[18:21], off
	global_store_dwordx4 v[42:43], v[22:25], off
	global_store_dwordx4 v[44:45], v[26:29], off
	global_load_dwordx4 v[14:17], v[50:51], off offset:528
	v_pk_mul_f32 v[18:19], v[174:175], v[178:179] op_sel_hi:[0,1]
	v_pk_mul_f32 v[20:21], v[174:175], v[176:177] op_sel_hi:[0,1]
	v_pk_mul_f32 v[22:23], v[168:169], v[2:3] op_sel_hi:[0,1]
	v_pk_mul_f32 v[24:25], v[168:169], v[4:5] op_sel_hi:[0,1]
	s_waitcnt vmcnt(0)
	v_mov_b32_e32 v250, s26
	v_min_u32_e32 v250, 0x55, v250
	v_mul_u32_u24_e32 v250, v250, v231
	v_mov_b32_e32 v251, 0
	v_lshl_add_u64 v[248:249], v[250:251], 0, v[252:253]
	global_load_dwordx4 v[248:251], v[248:249], off
	v_mov_b32_e32 v246, s28
	v_min_u32_e32 v246, 64, v246
	v_lshl_add_u32 v246, v246, 8, s55
	v_and_or_b32 v246, v166, 15, v246
	v_lshlrev_b32_e32 v246, 2, v246
	global_load_dword v240, v246, s[20:21]
	global_load_dword v241, v246, s[20:21] offset:64
	global_load_dword v242, v246, s[20:21] offset:128
	global_load_dword v243, v246, s[20:21] offset:192
	global_load_dword v244, v246, s[20:21] offset:512
	global_load_dword v245, v246, s[20:21] offset:576
	global_load_dword v247, v246, s[20:21] offset:704
	global_load_dword v246, v246, s[20:21] offset:640
	v_pk_mul_f32 v[4:5], v[12:13], v[16:17]
	v_pk_mul_f32 v[2:3], v[10:11], v[14:15]
	v_pk_mul_f32 v[8:9], v[8:9], v[16:17]
	v_pk_mul_f32 v[6:7], v[6:7], v[14:15]
	v_pk_mul_f32 v[12:13], v[24:25], v[16:17]
	v_pk_mul_f32 v[10:11], v[22:23], v[14:15]
	v_pk_mul_f32 v[16:17], v[20:21], v[16:17]
	v_pk_mul_f32 v[14:15], v[18:19], v[14:15]
	global_store_dwordx4 v[34:35], v[2:5], off offset:16
	global_store_dwordx4 v[36:37], v[6:9], off offset:16
	global_store_dwordx4 v[42:43], v[10:13], off offset:16
	global_store_dwordx4 v[44:45], v[14:17], off offset:16
	s_andn2_b64 vcc, exec, s[2:3]
	s_mov_b64 s[0:1], -1
	s_cbranch_vccnz .LBB0_1641
